# baseline (speedup 1.0000x reference)
_Z7xform_xPKfP15HIP_vector_typeIjLj4EE:
	s_load_dwordx4 s[4:7], s[0:1], 0x0
	s_lshr_b32 s8, s2, 2
	s_and_b32 s9, s2, 3
	v_and_b32_e32 v1, 15, v0
	v_lshrrev_b32_e32 v2, 4, v0
	v_lshrrev_b32_e32 v3, 3, v2
	v_and_b32_e32 v4, 7, v2
	s_lshl_b32 s10, s9, 3
	v_add_u32_e32 v5, s10, v4
	v_lshlrev_b32_e32 v5, 14, v5
	v_lshl_add_u32 v5, v3, 19, v5
	v_lshl_add_u32 v5, v1, 4, v5
	s_lshl_b32 s11, s8, 8
	v_add_u32_e32 v5, s11, v5
	v_xor_b32_e32 v40, v1, v3
	v_lshlrev_b32_e32 v42, 8, v2
	s_mov_b32 s14, 0x800000
	s_mov_b32 s15, 0x20000
	s_mov_b32 s18, 0x400000
	s_mov_b32 s19, 0x20000
	s_mov_b32 s20, 0x0
	s_mov_b32 s21, 0x100000
	s_mov_b32 s22, 0x200000
	s_mov_b32 s23, 0x300000
	s_mov_b32 s24, 0x400000
	s_mov_b32 s25, 0x500000
	s_mov_b32 s26, 0x600000
	s_mov_b32 s27, 0x700000
	s_waitcnt lgkmcnt(0)
	s_mov_b32 s12, s4
	s_and_b32 s13, s5, 0xffff
	s_mov_b32 s16, s6
	s_and_b32 s17, s7, 0xffff
	buffer_load_dwordx4 v[8:11], v5, s[12:15], s20 offen nt
	buffer_load_dwordx4 v[12:15], v5, s[12:15], s21 offen nt
	buffer_load_dwordx4 v[16:19], v5, s[12:15], s22 offen nt
	buffer_load_dwordx4 v[20:23], v5, s[12:15], s23 offen nt
	buffer_load_dwordx4 v[24:27], v5, s[12:15], s24 offen nt
	buffer_load_dwordx4 v[28:31], v5, s[12:15], s25 offen nt
	buffer_load_dwordx4 v[32:35], v5, s[12:15], s26 offen nt
	buffer_load_dwordx4 v[36:39], v5, s[12:15], s27 offen nt
	v_lshrrev_b32_e32 v43, 6, v0
	v_bfe_u32 v44, v0, 4, 2
	v_and_b32_e32 v45, 3, v1
	v_xor_b32_e32 v45, v43, v45
	v_lshlrev_b32_e32 v45, 4, v45
	v_lshl_add_u32 v45, v1, 11, v45
	v_lshl_add_u32 v45, v44, 2, v45
	v_lshrrev_b32_e32 v46, 2, v1
	s_lshl_b32 s28, s8, 16
	s_lshl_b32 s29, s9, 8
	s_add_u32 s28, s28, s29
	v_lshlrev_b32_e32 v48, 10, v2
	v_lshl_add_u32 v48, v1, 4, v48
	v_add_u32_e32 v48, s28, v48
	s_waitcnt vmcnt(7)
	v_xor_b32_e32 v41, 0, v40
	v_lshl_add_u32 v41, v41, 4, v42
	ds_write_b128 v41, v[8:11] offset:0
	s_waitcnt vmcnt(6)
	v_xor_b32_e32 v41, 2, v40
	v_lshl_add_u32 v41, v41, 4, v42
	ds_write_b128 v41, v[12:15] offset:4096
	s_waitcnt vmcnt(5)
	v_xor_b32_e32 v41, 4, v40
	v_lshl_add_u32 v41, v41, 4, v42
	ds_write_b128 v41, v[16:19] offset:8192
	s_waitcnt vmcnt(4)
	v_xor_b32_e32 v41, 6, v40
	v_lshl_add_u32 v41, v41, 4, v42
	ds_write_b128 v41, v[20:23] offset:12288
	s_waitcnt vmcnt(3)
	v_xor_b32_e32 v41, 8, v40
	v_lshl_add_u32 v41, v41, 4, v42
	ds_write_b128 v41, v[24:27] offset:16384
	s_waitcnt vmcnt(2)
	v_xor_b32_e32 v41, 10, v40
	v_lshl_add_u32 v41, v41, 4, v42
	ds_write_b128 v41, v[28:31] offset:20480
	s_waitcnt vmcnt(1)
	v_xor_b32_e32 v41, 12, v40
	v_lshl_add_u32 v41, v41, 4, v42
	ds_write_b128 v41, v[32:35] offset:24576
	s_waitcnt vmcnt(0)
	v_xor_b32_e32 v41, 14, v40
	v_lshl_add_u32 v41, v41, 4, v42
	ds_write_b128 v41, v[36:39] offset:28672
	s_waitcnt lgkmcnt(0)
	s_barrier
	v_xor_b32_e32 v47, 0, v46
	v_lshl_add_u32 v47, v47, 6, v45
	v_xor_b32_e32 v49, 1, v46
	v_lshl_add_u32 v49, v49, 6, v45
	ds_read2st64_b32 v[50:51], v47 offset0:0 offset1:1
	ds_read2st64_b32 v[52:53], v47 offset0:2 offset1:3
	ds_read2st64_b32 v[54:55], v47 offset0:4 offset1:5
	ds_read2st64_b32 v[56:57], v47 offset0:6 offset1:7
	ds_read2st64_b32 v[58:59], v49 offset0:0 offset1:1
	ds_read2st64_b32 v[60:61], v49 offset0:2 offset1:3
	ds_read2st64_b32 v[62:63], v49 offset0:4 offset1:5
	ds_read2st64_b32 v[64:65], v49 offset0:6 offset1:7
	s_waitcnt lgkmcnt(7)
	v_cvt_pk_f16_f32 v8, v50, v51
	s_waitcnt lgkmcnt(6)
	v_cvt_pk_f16_f32 v9, v52, v53
	s_waitcnt lgkmcnt(5)
	v_cvt_pk_f16_f32 v10, v54, v55
	s_waitcnt lgkmcnt(4)
	v_cvt_pk_f16_f32 v11, v56, v57
	s_mov_b32 s30, 0x0
	buffer_store_dwordx4 v[8:11], v48, s[16:19], s30 offen
	s_waitcnt lgkmcnt(3)
	v_cvt_pk_f16_f32 v12, v58, v59
	s_waitcnt lgkmcnt(2)
	v_cvt_pk_f16_f32 v13, v60, v61
	s_waitcnt lgkmcnt(1)
	v_cvt_pk_f16_f32 v14, v62, v63
	s_waitcnt lgkmcnt(0)
	v_cvt_pk_f16_f32 v15, v64, v65
	s_mov_b32 s30, 0x4000
	buffer_store_dwordx4 v[12:15], v48, s[16:19], s30 offen
	v_xor_b32_e32 v47, 2, v46
	v_lshl_add_u32 v47, v47, 6, v45
	v_xor_b32_e32 v49, 3, v46
	v_lshl_add_u32 v49, v49, 6, v45
	ds_read2st64_b32 v[50:51], v47 offset0:0 offset1:1
	ds_read2st64_b32 v[52:53], v47 offset0:2 offset1:3
	ds_read2st64_b32 v[54:55], v47 offset0:4 offset1:5
	ds_read2st64_b32 v[56:57], v47 offset0:6 offset1:7
	ds_read2st64_b32 v[58:59], v49 offset0:0 offset1:1
	ds_read2st64_b32 v[60:61], v49 offset0:2 offset1:3
	ds_read2st64_b32 v[62:63], v49 offset0:4 offset1:5
	ds_read2st64_b32 v[64:65], v49 offset0:6 offset1:7
	s_waitcnt lgkmcnt(7)
	v_cvt_pk_f16_f32 v16, v50, v51
	s_waitcnt lgkmcnt(6)
	v_cvt_pk_f16_f32 v17, v52, v53
	s_waitcnt lgkmcnt(5)
	v_cvt_pk_f16_f32 v18, v54, v55
	s_waitcnt lgkmcnt(4)
	v_cvt_pk_f16_f32 v19, v56, v57
	s_mov_b32 s30, 0x8000
	buffer_store_dwordx4 v[16:19], v48, s[16:19], s30 offen
	s_waitcnt lgkmcnt(3)
	v_cvt_pk_f16_f32 v20, v58, v59
	s_waitcnt lgkmcnt(2)
	v_cvt_pk_f16_f32 v21, v60, v61
	s_waitcnt lgkmcnt(1)
	v_cvt_pk_f16_f32 v22, v62, v63
	s_waitcnt lgkmcnt(0)
	v_cvt_pk_f16_f32 v23, v64, v65
	s_mov_b32 s30, 0xc000
	buffer_store_dwordx4 v[20:23], v48, s[16:19], s30 offen
	s_endpgm
